# norm+router phase: row sum-of-squares load and first x batch issued with the modulation loads; x batches prefetched one ahead
# speedup vs baseline: 1.0273x; 1.0026x over previous
.LBB0_776:
	s_waitcnt lgkmcnt(0)
	s_barrier
	s_and_saveexec_b64 s[0:1], s[42:43]
	ds_write_b32 v60, v2
	s_or_b64 exec, exec, s[0:1]
	s_add_i32 s0, s18, s2
	s_lshl_b32 s21, s0, 4
	s_cmpk_lt_i32 s0, 0x800
	s_cselect_b64 s[14:15], -1, 0
	s_and_b64 s[0:1], s[14:15], exec
	s_cselect_b32 s3, s21, 0
	s_lshl_b32 s0, s2, 4
	v_readlane_b32 s1, v251, 58
	s_add_i32 s0, s0, s1
	s_ashr_i32 s0, s0, 14
	s_min_i32 s0, s0, 1
	s_add_i32 s0, s0, s19
	v_mad_i64_i32 v[4:5], s[0:1], s0, v223, v[40:41]
	s_movk_i32 s0, 0x4000
	s_nop 0
	v_add_co_u32_e32 v6, vcc, s0, v4
	s_movk_i32 s0, 0x3000
	s_nop 0
	v_addc_co_u32_e32 v7, vcc, 0, v5, vcc
	v_add_co_u32_e32 v4, vcc, s0, v4
	v_or_b32_e32 v8, s3, v3
	s_nop 0
	v_addc_co_u32_e32 v5, vcc, 0, v5, vcc
	global_load_dword v10, v[6:7], off
	s_nop 0
	global_load_dword v6, v[6:7], off offset:2048
	s_nop 0
	global_load_dword v7, v[4:5], off
	global_load_dword v11, v[4:5], off offset:2048
	global_load_dword v12, v[36:37], off
	global_load_dword v13, v[38:39], off offset:2048
	v_ashrrev_i32_e32 v9, 31, v8
	v_lshlrev_b64 v[4:5], 6, v[8:9]
	v_lshl_add_u64 v[4:5], v[32:33], 0, v[4:5]
	global_load_dwordx4 v[146:149], v[4:5], off
	v_lshlrev_b64 v[150:151], 11, v[8:9]
	v_lshl_add_u64 v[144:145], v[44:45], 0, v[150:151]
	v_lshl_add_u64 v[144:145], s[8:9], 0, v[144:145]
	v_add_co_u32_e32 v144, vcc, 0x26600000, v144
	s_nop 1
	v_addc_co_u32_e32 v145, vcc, 0, v145, vcc
	s_nop 0
	global_load_dwordx4 v[112:115], v[144:145], off
	global_load_dwordx4 v[116:119], v[144:145], off offset:64
	global_load_dwordx4 v[120:123], v[144:145], off offset:128
	global_load_dwordx4 v[124:127], v[144:145], off offset:192
	global_load_dwordx4 v[128:131], v[144:145], off offset:256
	global_load_dwordx4 v[132:135], v[144:145], off offset:320
	global_load_dwordx4 v[136:139], v[144:145], off offset:384
	global_load_dwordx4 v[140:143], v[144:145], off offset:448
	s_mov_b32 s0, -8
	v_mov_b32_e32 v65, v58
	v_mov_b32_e32 v66, v62
	s_waitcnt vmcnt(14)
	v_add_f32_e32 v10, 1.0, v10
	s_waitcnt vmcnt(13)
	v_add_f32_e32 v6, 1.0, v6
	s_waitcnt vmcnt(11)
	ds_write2st64_b32 v59, v7, v11 offset0:145 offset1:153
	s_waitcnt vmcnt(10)
	v_mul_f32_e32 v7, v12, v10
	s_waitcnt vmcnt(9)
	v_mul_f32_e32 v6, v13, v6
	ds_write2st64_b32 v59, v7, v6 offset0:129 offset1:137
	s_waitcnt lgkmcnt(0)
	s_barrier
	s_waitcnt vmcnt(8)
	v_mov_b32_e32 v4, v146
	v_mov_b32_e32 v5, v147
	v_mov_b32_e32 v6, v148
	v_mov_b32_e32 v7, v149
	v_mov_b32_e32 v10, v5
	v_mov_b32_e32 v11, v6
	v_mov_b32_e32 v5, v7
	v_pk_add_f32 v[4:5], v[10:11], v[4:5]
	v_lshlrev_b64 v[10:11], 10, v[8:9]
	v_add_f32_e32 v5, v4, v5
	ds_bpermute_b32 v6, v56, v5
	v_mov_b32_e32 v4, 0
	v_lshlrev_b64 v[8:9], 11, v[8:9]
	v_lshl_add_u64 v[48:49], v[44:45], 0, v[8:9]
	v_lshl_add_u64 v[50:51], v[34:35], 0, v[10:11]
	s_waitcnt lgkmcnt(0)
	v_add_f32_e32 v7, v5, v6
	ds_bpermute_b32 v12, v57, v7
	v_mov_b32_e32 v5, v4
	v_mov_b32_e32 v6, v4
	s_waitcnt lgkmcnt(0)
	v_add_f32_e32 v7, v7, v12
	v_fmamk_f32 v7, v7, 0x3a800000, v210
	v_rsq_f32_e32 v46, v7
	v_mov_b32_e32 v7, v4
	v_mov_b32_e32 v47, v46
	v_mov_b32_e32 v52, v46
	v_mov_b32_e32 v53, v46
	s_waitcnt vmcnt(0)
.LBB0_779:
	v_mov_b32_e32 v68, v112
	v_mov_b32_e32 v69, v113
	v_mov_b32_e32 v70, v114
	v_mov_b32_e32 v71, v115
	v_mov_b32_e32 v72, v116
	v_mov_b32_e32 v73, v117
	v_mov_b32_e32 v74, v118
	v_mov_b32_e32 v75, v119
	v_mov_b32_e32 v28, v120
	v_mov_b32_e32 v29, v121
	v_mov_b32_e32 v30, v122
	v_mov_b32_e32 v31, v123
	v_mov_b32_e32 v24, v124
	v_mov_b32_e32 v25, v125
	v_mov_b32_e32 v26, v126
	v_mov_b32_e32 v27, v127
	v_mov_b32_e32 v20, v128
	v_mov_b32_e32 v21, v129
	v_mov_b32_e32 v22, v130
	v_mov_b32_e32 v23, v131
	v_mov_b32_e32 v16, v132
	v_mov_b32_e32 v17, v133
	v_mov_b32_e32 v18, v134
	v_mov_b32_e32 v19, v135
	v_mov_b32_e32 v12, v136
	v_mov_b32_e32 v13, v137
	v_mov_b32_e32 v14, v138
	v_mov_b32_e32 v15, v139
	v_mov_b32_e32 v8, v140
	v_mov_b32_e32 v9, v141
	v_mov_b32_e32 v10, v142
	v_mov_b32_e32 v11, v143
	s_mov_b32 s1, 0xd400000
	s_mov_b64 s[2:3], 0x200
	s_add_i32 s0, s0, 8
	v_lshl_add_u64 v[48:49], v[48:49], 0, s[2:3]
	s_mov_b64 s[2:3], 0x100
	s_cmp_gt_u32 s0, 23
	s_cbranch_scc1 .LPF_skip
	v_lshl_add_u64 v[144:145], s[8:9], 0, v[48:49]
	v_add_co_u32_e32 v144, vcc, 0x26600000, v144
	s_nop 1
	v_addc_co_u32_e32 v145, vcc, 0, v145, vcc
	s_nop 0
	global_load_dwordx4 v[112:115], v[144:145], off
	global_load_dwordx4 v[116:119], v[144:145], off offset:64
	global_load_dwordx4 v[120:123], v[144:145], off offset:128
	global_load_dwordx4 v[124:127], v[144:145], off offset:192
	global_load_dwordx4 v[128:131], v[144:145], off offset:256
	global_load_dwordx4 v[132:135], v[144:145], off offset:320
	global_load_dwordx4 v[136:139], v[144:145], off offset:384
	global_load_dwordx4 v[140:143], v[144:145], off offset:448
.LPF_skip:
	v_lshlrev_b32_e32 v54, 16, v68
	v_and_b32_e32 v55, 0xffff0000, v68
	v_lshlrev_b32_e32 v88, 16, v69
	v_and_b32_e32 v89, 0xffff0000, v69
	v_lshlrev_b32_e32 v90, 16, v70
	v_and_b32_e32 v91, 0xffff0000, v70
	v_lshlrev_b32_e32 v92, 16, v71
	v_and_b32_e32 v93, 0xffff0000, v71
	ds_read_b128 v[68:71], v66
	ds_read_b128 v[76:79], v66 offset:16
	ds_read_b128 v[80:83], v66 offset:4096
	ds_read_b128 v[84:87], v66 offset:4112
	v_pk_mul_f32 v[54:55], v[46:47], v[54:55]
	v_pk_mul_f32 v[88:89], v[52:53], v[88:89]
	s_waitcnt lgkmcnt(1)
	v_pk_fma_f32 v[54:55], v[54:55], v[68:69], v[80:81]
	v_pk_mul_f32 v[68:69], v[46:47], v[90:91]
	v_mov_b32_e32 v80, v2
	s_waitcnt lgkmcnt(0)
	v_pk_fma_f32 v[76:77], v[68:69], v[76:77], v[84:85]
	v_mov_b32_e32 v81, v2
	v_cvt_pk_fp8_f32 v80, v54, v55
	v_cvt_pk_fp8_f32 v81, v76, v77
	v_pk_fma_f32 v[82:83], v[88:89], v[70:71], v[82:83]
	v_pk_mul_f32 v[70:71], v[52:53], v[92:93]
	v_cvt_pk_bf16_f32 v68, v54, v55
	v_pk_fma_f32 v[78:79], v[70:71], v[78:79], v[86:87]
	v_cvt_pk_bf16_f32 v69, v82, v83
	v_cvt_pk_bf16_f32 v70, v76, v77
	v_cvt_pk_bf16_f32 v71, v78, v79
	v_cvt_pk_fp8_f32 v80, v82, v83 op_sel:[0,0,1]
	v_cvt_pk_fp8_f32 v81, v78, v79 op_sel:[0,0,1]
	ds_read_b128 v[76:79], v65
	v_lshl_add_u64 v[54:55], s[8:9], 0, v[50:51]
	v_add_co_u32_e32 v54, vcc, s1, v54
	s_waitcnt lgkmcnt(0)
	v_mfma_f32_16x16x32_bf16 v[4:7], v[68:71], v[76:79], v[4:7]
	v_addc_co_u32_e32 v55, vcc, 0, v55, vcc
	global_store_dwordx2 v[54:55], v[80:81], off
	v_lshlrev_b32_e32 v84, 16, v72
	v_and_b32_e32 v85, 0xffff0000, v72
	v_lshlrev_b32_e32 v86, 16, v73
	v_and_b32_e32 v87, 0xffff0000, v73
	v_lshlrev_b32_e32 v88, 16, v74
	v_and_b32_e32 v89, 0xffff0000, v74
	v_lshlrev_b32_e32 v90, 16, v75
	v_and_b32_e32 v91, 0xffff0000, v75
	ds_read_b128 v[68:71], v66 offset:128
	ds_read_b128 v[72:75], v66 offset:144
	ds_read_b128 v[76:79], v66 offset:4224
	ds_read_b128 v[80:83], v66 offset:4240
	v_pk_mul_f32 v[84:85], v[46:47], v[84:85]
	v_pk_mul_f32 v[86:87], v[52:53], v[86:87]
	v_lshl_add_u64 v[50:51], v[50:51], 0, s[2:3]
	s_waitcnt lgkmcnt(1)
	v_pk_fma_f32 v[76:77], v[84:85], v[68:69], v[76:77]
	v_pk_mul_f32 v[68:69], v[46:47], v[88:89]
	v_pk_fma_f32 v[78:79], v[86:87], v[70:71], v[78:79]
	s_waitcnt lgkmcnt(0)
	v_pk_fma_f32 v[72:73], v[68:69], v[72:73], v[80:81]
	v_mov_b32_e32 v80, v2
	v_mov_b32_e32 v81, v2
	v_cvt_pk_fp8_f32 v80, v76, v77
	v_cvt_pk_fp8_f32 v81, v72, v73
	v_pk_mul_f32 v[70:71], v[52:53], v[90:91]
	v_cvt_pk_bf16_f32 v68, v76, v77
	v_pk_fma_f32 v[74:75], v[70:71], v[74:75], v[82:83]
	v_cvt_pk_bf16_f32 v69, v78, v79
	v_cvt_pk_bf16_f32 v70, v72, v73
	v_cvt_pk_bf16_f32 v71, v74, v75
	v_cvt_pk_fp8_f32 v80, v78, v79 op_sel:[0,0,1]
	v_cvt_pk_fp8_f32 v81, v74, v75 op_sel:[0,0,1]
	ds_read_b128 v[72:75], v65 offset:64
	s_waitcnt lgkmcnt(0)
	v_mfma_f32_16x16x32_bf16 v[4:7], v[68:71], v[72:75], v[4:7]
	global_store_dwordx2 v[54:55], v[80:81], off offset:32
	v_lshlrev_b32_e32 v80, 16, v28
	v_and_b32_e32 v81, 0xffff0000, v28
	v_lshlrev_b32_e32 v82, 16, v29
	v_and_b32_e32 v83, 0xffff0000, v29
	v_lshlrev_b32_e32 v84, 16, v30
	v_and_b32_e32 v85, 0xffff0000, v30
	v_lshlrev_b32_e32 v86, 16, v31
	v_and_b32_e32 v87, 0xffff0000, v31
	ds_read_b128 v[28:31], v66 offset:256
	ds_read_b128 v[68:71], v66 offset:272
	ds_read_b128 v[72:75], v66 offset:4352
	ds_read_b128 v[76:79], v66 offset:4368
	v_pk_mul_f32 v[80:81], v[46:47], v[80:81]
	v_pk_mul_f32 v[82:83], v[52:53], v[82:83]
	s_waitcnt lgkmcnt(1)
	v_pk_fma_f32 v[72:73], v[80:81], v[28:29], v[72:73]
	v_pk_mul_f32 v[28:29], v[46:47], v[84:85]
	v_pk_fma_f32 v[74:75], v[82:83], v[30:31], v[74:75]
	s_waitcnt lgkmcnt(0)
	v_pk_fma_f32 v[68:69], v[28:29], v[68:69], v[76:77]
	v_mov_b32_e32 v76, v2
	v_mov_b32_e32 v77, v2
	v_cvt_pk_fp8_f32 v76, v72, v73
	v_cvt_pk_fp8_f32 v77, v68, v69
	v_pk_mul_f32 v[30:31], v[52:53], v[86:87]
	v_cvt_pk_bf16_f32 v28, v72, v73
	v_pk_fma_f32 v[70:71], v[30:31], v[70:71], v[78:79]
	v_cvt_pk_bf16_f32 v29, v74, v75
	v_cvt_pk_bf16_f32 v30, v68, v69
	v_cvt_pk_bf16_f32 v31, v70, v71
	v_cvt_pk_fp8_f32 v76, v74, v75 op_sel:[0,0,1]
	v_cvt_pk_fp8_f32 v77, v70, v71 op_sel:[0,0,1]
	ds_read_b128 v[68:71], v65 offset:128
	s_waitcnt lgkmcnt(0)
	v_mfma_f32_16x16x32_bf16 v[4:7], v[28:31], v[68:71], v[4:7]
	global_store_dwordx2 v[54:55], v[76:77], off offset:64
	v_lshlrev_b32_e32 v76, 16, v24
	v_and_b32_e32 v77, 0xffff0000, v24
	v_lshlrev_b32_e32 v78, 16, v25
	v_and_b32_e32 v79, 0xffff0000, v25
	v_lshlrev_b32_e32 v80, 16, v26
	v_and_b32_e32 v81, 0xffff0000, v26
	v_lshlrev_b32_e32 v82, 16, v27
	v_and_b32_e32 v83, 0xffff0000, v27
	ds_read_b128 v[24:27], v66 offset:384
	ds_read_b128 v[28:31], v66 offset:400
	ds_read_b128 v[68:71], v66 offset:4480
	ds_read_b128 v[72:75], v66 offset:4496
	v_pk_mul_f32 v[76:77], v[46:47], v[76:77]
	v_pk_mul_f32 v[78:79], v[52:53], v[78:79]
	s_waitcnt lgkmcnt(1)
	v_pk_fma_f32 v[68:69], v[76:77], v[24:25], v[68:69]
	v_pk_mul_f32 v[24:25], v[46:47], v[80:81]
	v_pk_fma_f32 v[70:71], v[78:79], v[26:27], v[70:71]
	s_waitcnt lgkmcnt(0)
	v_pk_fma_f32 v[28:29], v[24:25], v[28:29], v[72:73]
	v_mov_b32_e32 v72, v2
	v_mov_b32_e32 v73, v2
	v_cvt_pk_fp8_f32 v72, v68, v69
	v_cvt_pk_fp8_f32 v73, v28, v29
	v_pk_mul_f32 v[26:27], v[52:53], v[82:83]
	v_cvt_pk_bf16_f32 v24, v68, v69
	v_pk_fma_f32 v[30:31], v[26:27], v[30:31], v[74:75]
	v_cvt_pk_bf16_f32 v25, v70, v71
	v_cvt_pk_bf16_f32 v26, v28, v29
	v_cvt_pk_bf16_f32 v27, v30, v31
	v_cvt_pk_fp8_f32 v72, v70, v71 op_sel:[0,0,1]
	v_cvt_pk_fp8_f32 v73, v30, v31 op_sel:[0,0,1]
	ds_read_b128 v[28:31], v65 offset:192
	s_waitcnt lgkmcnt(0)
	v_mfma_f32_16x16x32_bf16 v[4:7], v[24:27], v[28:31], v[4:7]
	global_store_dwordx2 v[54:55], v[72:73], off offset:96
	v_lshlrev_b32_e32 v72, 16, v20
	v_and_b32_e32 v73, 0xffff0000, v20
	v_lshlrev_b32_e32 v74, 16, v21
	v_and_b32_e32 v75, 0xffff0000, v21
	v_lshlrev_b32_e32 v76, 16, v22
	v_and_b32_e32 v77, 0xffff0000, v22
	v_lshlrev_b32_e32 v78, 16, v23
	v_and_b32_e32 v79, 0xffff0000, v23
	ds_read_b128 v[20:23], v66 offset:512
	ds_read_b128 v[24:27], v66 offset:528
	ds_read_b128 v[28:31], v66 offset:4608
	ds_read_b128 v[68:71], v66 offset:4624
	v_pk_mul_f32 v[72:73], v[46:47], v[72:73]
	v_pk_mul_f32 v[74:75], v[52:53], v[74:75]
	s_waitcnt lgkmcnt(1)
	v_pk_fma_f32 v[28:29], v[72:73], v[20:21], v[28:29]
	v_pk_mul_f32 v[20:21], v[46:47], v[76:77]
	v_pk_fma_f32 v[30:31], v[74:75], v[22:23], v[30:31]
	s_waitcnt lgkmcnt(0)
	v_pk_fma_f32 v[24:25], v[20:21], v[24:25], v[68:69]
	v_mov_b32_e32 v68, v2
	v_mov_b32_e32 v69, v2
	v_cvt_pk_fp8_f32 v68, v28, v29
	v_cvt_pk_fp8_f32 v69, v24, v25
	v_pk_mul_f32 v[22:23], v[52:53], v[78:79]
	v_cvt_pk_bf16_f32 v20, v28, v29
	v_pk_fma_f32 v[26:27], v[22:23], v[26:27], v[70:71]
	v_cvt_pk_bf16_f32 v21, v30, v31
	v_cvt_pk_bf16_f32 v22, v24, v25
	v_cvt_pk_bf16_f32 v23, v26, v27
	v_cvt_pk_fp8_f32 v68, v30, v31 op_sel:[0,0,1]
	v_cvt_pk_fp8_f32 v69, v26, v27 op_sel:[0,0,1]
	ds_read_b128 v[24:27], v65 offset:256
	s_waitcnt lgkmcnt(0)
	v_mfma_f32_16x16x32_bf16 v[4:7], v[20:23], v[24:27], v[4:7]
	global_store_dwordx2 v[54:55], v[68:69], off offset:128
	v_lshlrev_b32_e32 v68, 16, v16
	v_and_b32_e32 v69, 0xffff0000, v16
	v_lshlrev_b32_e32 v70, 16, v17
	v_and_b32_e32 v71, 0xffff0000, v17
	v_lshlrev_b32_e32 v72, 16, v18
	v_and_b32_e32 v73, 0xffff0000, v18
	v_lshlrev_b32_e32 v74, 16, v19
	v_and_b32_e32 v75, 0xffff0000, v19
	ds_read_b128 v[16:19], v66 offset:640
	ds_read_b128 v[20:23], v66 offset:656
	ds_read_b128 v[24:27], v66 offset:4736
	ds_read_b128 v[28:31], v66 offset:4752
	v_pk_mul_f32 v[68:69], v[46:47], v[68:69]
	v_pk_mul_f32 v[70:71], v[52:53], v[70:71]
	s_waitcnt lgkmcnt(1)
	v_pk_fma_f32 v[24:25], v[68:69], v[16:17], v[24:25]
	v_pk_mul_f32 v[16:17], v[46:47], v[72:73]
	v_pk_fma_f32 v[26:27], v[70:71], v[18:19], v[26:27]
	s_waitcnt lgkmcnt(0)
	v_pk_fma_f32 v[20:21], v[16:17], v[20:21], v[28:29]
	v_mov_b32_e32 v28, v2
	v_mov_b32_e32 v29, v2
	v_cvt_pk_fp8_f32 v28, v24, v25
	v_cvt_pk_fp8_f32 v29, v20, v21
	v_pk_mul_f32 v[18:19], v[52:53], v[74:75]
	v_cvt_pk_bf16_f32 v16, v24, v25
	v_pk_fma_f32 v[22:23], v[18:19], v[22:23], v[30:31]
	v_cvt_pk_bf16_f32 v17, v26, v27
	v_cvt_pk_bf16_f32 v18, v20, v21
	v_cvt_pk_bf16_f32 v19, v22, v23
	v_cvt_pk_fp8_f32 v28, v26, v27 op_sel:[0,0,1]
	v_cvt_pk_fp8_f32 v29, v22, v23 op_sel:[0,0,1]
	ds_read_b128 v[20:23], v65 offset:320
	s_waitcnt lgkmcnt(0)
	v_mfma_f32_16x16x32_bf16 v[4:7], v[16:19], v[20:23], v[4:7]
	global_store_dwordx2 v[54:55], v[28:29], off offset:160
	v_lshlrev_b32_e32 v28, 16, v12
	v_and_b32_e32 v29, 0xffff0000, v12
	v_lshlrev_b32_e32 v30, 16, v13
	v_and_b32_e32 v31, 0xffff0000, v13
	v_lshlrev_b32_e32 v68, 16, v14
	v_and_b32_e32 v69, 0xffff0000, v14
	v_lshlrev_b32_e32 v70, 16, v15
	v_and_b32_e32 v71, 0xffff0000, v15
	ds_read_b128 v[12:15], v66 offset:768
	ds_read_b128 v[16:19], v66 offset:784
	ds_read_b128 v[20:23], v66 offset:4864
	ds_read_b128 v[24:27], v66 offset:4880
	v_pk_mul_f32 v[28:29], v[46:47], v[28:29]
	v_pk_mul_f32 v[30:31], v[52:53], v[30:31]
	s_waitcnt lgkmcnt(1)
	v_pk_fma_f32 v[20:21], v[28:29], v[12:13], v[20:21]
	v_pk_mul_f32 v[12:13], v[46:47], v[68:69]
	v_pk_fma_f32 v[22:23], v[30:31], v[14:15], v[22:23]
	s_waitcnt lgkmcnt(0)
	v_pk_fma_f32 v[16:17], v[12:13], v[16:17], v[24:25]
	v_mov_b32_e32 v24, v2
	v_mov_b32_e32 v25, v2
	v_cvt_pk_fp8_f32 v24, v20, v21
	v_cvt_pk_fp8_f32 v25, v16, v17
	v_pk_mul_f32 v[14:15], v[52:53], v[70:71]
	v_cvt_pk_bf16_f32 v12, v20, v21
	v_pk_fma_f32 v[18:19], v[14:15], v[18:19], v[26:27]
	v_cvt_pk_bf16_f32 v13, v22, v23
	v_cvt_pk_bf16_f32 v14, v16, v17
	v_cvt_pk_bf16_f32 v15, v18, v19
	v_cvt_pk_fp8_f32 v24, v22, v23 op_sel:[0,0,1]
	v_cvt_pk_fp8_f32 v25, v18, v19 op_sel:[0,0,1]
	ds_read_b128 v[16:19], v65 offset:384
	s_waitcnt lgkmcnt(0)
	v_mfma_f32_16x16x32_bf16 v[4:7], v[12:15], v[16:19], v[4:7]
	global_store_dwordx2 v[54:55], v[24:25], off offset:192
	v_lshlrev_b32_e32 v24, 16, v8
	v_and_b32_e32 v25, 0xffff0000, v8
	v_lshlrev_b32_e32 v26, 16, v9
	v_and_b32_e32 v27, 0xffff0000, v9
	v_lshlrev_b32_e32 v28, 16, v10
	v_and_b32_e32 v29, 0xffff0000, v10
	v_lshlrev_b32_e32 v30, 16, v11
	v_and_b32_e32 v31, 0xffff0000, v11
	ds_read_b128 v[8:11], v66 offset:896
	ds_read_b128 v[12:15], v66 offset:912
	ds_read_b128 v[16:19], v66 offset:4992
	ds_read_b128 v[20:23], v66 offset:5008
	v_pk_mul_f32 v[24:25], v[46:47], v[24:25]
	v_pk_mul_f32 v[26:27], v[52:53], v[26:27]
	v_add_u32_e32 v66, 0x400, v66
	s_waitcnt lgkmcnt(1)
	v_pk_fma_f32 v[16:17], v[24:25], v[8:9], v[16:17]
	v_pk_mul_f32 v[8:9], v[46:47], v[28:29]
	v_pk_fma_f32 v[18:19], v[26:27], v[10:11], v[18:19]
	s_waitcnt lgkmcnt(0)
	v_pk_fma_f32 v[12:13], v[8:9], v[12:13], v[20:21]
	v_mov_b32_e32 v21, v2
	v_cvt_pk_fp8_f32 v21, v12, v13
	v_pk_mul_f32 v[10:11], v[52:53], v[30:31]
	v_cvt_pk_bf16_f32 v8, v16, v17
	v_pk_fma_f32 v[14:15], v[10:11], v[14:15], v[22:23]
	v_cvt_pk_bf16_f32 v9, v18, v19
	v_cvt_pk_bf16_f32 v10, v12, v13
	v_cvt_pk_bf16_f32 v11, v14, v15
	v_mov_b32_e32 v20, v2
	v_cvt_pk_fp8_f32 v21, v14, v15 op_sel:[0,0,1]
	ds_read_b128 v[12:15], v65 offset:448
	v_cvt_pk_fp8_f32 v20, v16, v17
	s_waitcnt lgkmcnt(0)
	v_mfma_f32_16x16x32_bf16 v[4:7], v[8:11], v[12:15], v[4:7]
	v_cvt_pk_fp8_f32 v20, v18, v19 op_sel:[0,0,1]
	v_add_u32_e32 v65, 0x200, v65
	global_store_dwordx2 v[54:55], v[20:21], off offset:224
	s_waitcnt vmcnt(8)
	s_cbranch_scc0 .LBB0_779
	v_add_u32_e32 v8, 0xa000, v63
	s_nop 2
	ds_write2_b32 v8, v4, v5 offset0:64 offset1:81
	ds_write2_b32 v8, v6, v7 offset0:98 offset1:115
	s_waitcnt lgkmcnt(0)
	v_mov_b32_e32 v6, 0
	v_mov_b32_e32 v50, 0
	v_mov_b32_e32 v5, 0
	v_mov_b32_e32 v4, 0
	s_and_saveexec_b64 s[16:17], s[40:41]
	s_cbranch_execz .LBB0_782
	v_add_u32_e32 v4, 0xa100, v64
	ds_read2_b32 v[4:5], v4 offset1:1
	s_mov_b32 s4, 0xf149f2ca
	s_waitcnt lgkmcnt(0)
	v_mul_f32_e32 v4, 0xbfb8aa3b, v4
	v_mul_f32_e32 v5, 0xbfb8aa3b, v5
	v_exp_f32_e32 v4, v4
	v_exp_f32_e32 v5, v5
	s_nop 0
	v_pk_add_f32 v[4:5], v[4:5], 1.0 op_sel_hi:[1,0]
	s_nop 0
	v_div_scale_f32 v6, s[0:1], v5, v5, 1.0
	v_rcp_f32_e32 v7, v6
	s_nop 0
	v_fma_f32 v8, -v6, v7, 1.0
	v_fmac_f32_e32 v7, v8, v7
	v_div_scale_f32 v8, vcc, 1.0, v5, 1.0
	v_mul_f32_e32 v9, v8, v7
	v_fma_f32 v10, -v6, v9, v8
	v_fmac_f32_e32 v9, v10, v7
	v_fma_f32 v6, -v6, v9, v8
	v_div_fmas_f32 v6, v6, v7, v9
	v_div_fixup_f32 v17, v6, v5, 1.0
	v_div_scale_f32 v5, s[0:1], v4, v4, 1.0
	v_rcp_f32_e32 v6, v5
	s_nop 0
	v_fma_f32 v7, -v5, v6, 1.0
	v_fmac_f32_e32 v6, v7, v6
	v_div_scale_f32 v7, vcc, 1.0, v4, 1.0
	v_mul_f32_e32 v8, v7, v6
	v_fma_f32 v9, -v5, v8, v7
	v_fmac_f32_e32 v8, v9, v6
	v_fma_f32 v5, -v5, v8, v7
	v_div_fmas_f32 v5, v5, v6, v8
	v_div_fixup_f32 v16, v5, v4, 1.0
	global_load_dwordx4 v[4:7], v2, s[6:7] offset:48
	global_load_dwordx4 v[8:11], v2, s[6:7] offset:32
	global_load_dwordx4 v[12:15], v2, s[6:7] offset:16
	global_load_dwordx4 v[20:23], v2, s[6:7]
	s_waitcnt vmcnt(0)
	v_pk_add_f32 v[18:19], v[20:21], v[16:17]
	v_add_u32_e32 v20, 0xa108, v64
	ds_read2_b32 v[20:21], v20 offset1:1
	s_waitcnt lgkmcnt(0)
	v_mul_f32_e32 v20, 0xbfb8aa3b, v20
	v_mul_f32_e32 v21, 0xbfb8aa3b, v21
	v_exp_f32_e32 v20, v20
	v_exp_f32_e32 v21, v21
	s_nop 0
	v_pk_add_f32 v[20:21], v[20:21], 1.0 op_sel_hi:[1,0]
	s_nop 0
	v_div_scale_f32 v24, s[0:1], v21, v21, 1.0
	v_rcp_f32_e32 v25, v24
	s_nop 0
	v_fma_f32 v26, -v24, v25, 1.0
	v_fmac_f32_e32 v25, v26, v25
	v_div_scale_f32 v26, vcc, 1.0, v21, 1.0
	v_mul_f32_e32 v27, v26, v25
	v_fma_f32 v28, -v24, v27, v26
	v_fmac_f32_e32 v27, v28, v25
	v_fma_f32 v24, -v24, v27, v26
	v_div_fmas_f32 v24, v24, v25, v27
	v_div_fixup_f32 v21, v24, v21, 1.0
	v_div_scale_f32 v24, s[0:1], v20, v20, 1.0
	v_rcp_f32_e32 v25, v24
	s_nop 0
	v_fma_f32 v26, -v24, v25, 1.0
	v_fmac_f32_e32 v25, v26, v25
	v_div_scale_f32 v26, vcc, 1.0, v20, 1.0
	v_mul_f32_e32 v27, v26, v25
	v_fma_f32 v28, -v24, v27, v26
	v_fmac_f32_e32 v27, v28, v25
	v_fma_f32 v24, -v24, v27, v26
	v_div_fmas_f32 v24, v24, v25, v27
	v_div_fixup_f32 v20, v24, v20, 1.0
	v_add_u32_e32 v24, 0xa110, v64
	ds_read2_b32 v[24:25], v24 offset1:1
	v_pk_add_f32 v[22:23], v[22:23], v[20:21]
	s_waitcnt lgkmcnt(0)
	v_mul_f32_e32 v24, 0xbfb8aa3b, v24
	v_mul_f32_e32 v25, 0xbfb8aa3b, v25
	v_exp_f32_e32 v24, v24
	v_exp_f32_e32 v25, v25
	s_nop 0
	v_pk_add_f32 v[24:25], v[24:25], 1.0 op_sel_hi:[1,0]
	s_nop 0
	v_div_scale_f32 v26, s[0:1], v25, v25, 1.0
	v_rcp_f32_e32 v27, v26
	s_nop 0
	v_fma_f32 v28, -v26, v27, 1.0
	v_fmac_f32_e32 v27, v28, v27
	v_div_scale_f32 v28, vcc, 1.0, v25, 1.0
	v_mul_f32_e32 v29, v28, v27
	v_fma_f32 v30, -v26, v29, v28
	v_fmac_f32_e32 v29, v30, v27
	v_fma_f32 v26, -v26, v29, v28
	v_div_fmas_f32 v26, v26, v27, v29
	v_div_fixup_f32 v25, v26, v25, 1.0
	v_div_scale_f32 v26, s[0:1], v24, v24, 1.0
	v_rcp_f32_e32 v27, v26
	s_nop 0
	v_fma_f32 v28, -v26, v27, 1.0
	v_fmac_f32_e32 v27, v28, v27
	v_div_scale_f32 v28, vcc, 1.0, v24, 1.0
	v_mul_f32_e32 v29, v28, v27
	v_fma_f32 v30, -v26, v29, v28
	v_fmac_f32_e32 v29, v30, v27
	v_fma_f32 v26, -v26, v29, v28
	v_div_fmas_f32 v26, v26, v27, v29
	v_div_fixup_f32 v24, v26, v24, 1.0
	v_add_u32_e32 v26, 0xa118, v64
	ds_read2_b32 v[26:27], v26 offset1:1
	v_pk_add_f32 v[12:13], v[12:13], v[24:25]
	s_waitcnt lgkmcnt(0)
	v_mul_f32_e32 v26, 0xbfb8aa3b, v26
	v_mul_f32_e32 v27, 0xbfb8aa3b, v27
	v_exp_f32_e32 v26, v26
	v_exp_f32_e32 v27, v27
	s_nop 0
	v_pk_add_f32 v[26:27], v[26:27], 1.0 op_sel_hi:[1,0]
	s_nop 0
	v_div_scale_f32 v28, s[0:1], v27, v27, 1.0
	v_rcp_f32_e32 v29, v28
	s_nop 0
	v_fma_f32 v30, -v28, v29, 1.0
	v_fmac_f32_e32 v29, v30, v29
	v_div_scale_f32 v30, vcc, 1.0, v27, 1.0
	v_mul_f32_e32 v31, v30, v29
	v_fma_f32 v46, -v28, v31, v30
	v_fmac_f32_e32 v31, v46, v29
	v_fma_f32 v28, -v28, v31, v30
	v_div_fmas_f32 v28, v28, v29, v31
	v_div_fixup_f32 v27, v28, v27, 1.0
	v_div_scale_f32 v28, s[0:1], v26, v26, 1.0
	v_rcp_f32_e32 v29, v28
	s_nop 0
	v_fma_f32 v30, -v28, v29, 1.0
	v_fmac_f32_e32 v29, v30, v29
	v_div_scale_f32 v30, vcc, 1.0, v26, 1.0
	v_mul_f32_e32 v31, v30, v29
	v_fma_f32 v46, -v28, v31, v30
	v_fmac_f32_e32 v31, v46, v29
	v_fma_f32 v28, -v28, v31, v30
	v_div_fmas_f32 v28, v28, v29, v31
	v_div_fixup_f32 v26, v28, v26, 1.0
	v_add_u32_e32 v28, 0xa120, v64
	ds_read2_b32 v[28:29], v28 offset1:1
	v_pk_add_f32 v[14:15], v[14:15], v[26:27]
	s_waitcnt lgkmcnt(0)
	v_mul_f32_e32 v28, 0xbfb8aa3b, v28
	v_mul_f32_e32 v29, 0xbfb8aa3b, v29
	v_exp_f32_e32 v28, v28
	v_exp_f32_e32 v29, v29
	s_nop 0
	v_pk_add_f32 v[28:29], v[28:29], 1.0 op_sel_hi:[1,0]
	s_nop 0
	v_div_scale_f32 v30, s[0:1], v29, v29, 1.0
	v_rcp_f32_e32 v31, v30
	s_nop 0
	v_fma_f32 v46, -v30, v31, 1.0
	v_fmac_f32_e32 v31, v46, v31
	v_div_scale_f32 v46, vcc, 1.0, v29, 1.0
	v_mul_f32_e32 v47, v46, v31
	v_fma_f32 v48, -v30, v47, v46
	v_fmac_f32_e32 v47, v48, v31
	v_fma_f32 v30, -v30, v47, v46
	v_div_fmas_f32 v30, v30, v31, v47
	v_div_fixup_f32 v29, v30, v29, 1.0
	v_div_scale_f32 v30, s[0:1], v28, v28, 1.0
	v_rcp_f32_e32 v31, v30
	s_nop 0
	v_fma_f32 v46, -v30, v31, 1.0
	v_fmac_f32_e32 v31, v46, v31
	v_div_scale_f32 v46, vcc, 1.0, v28, 1.0
	v_mul_f32_e32 v47, v46, v31
	v_fma_f32 v48, -v30, v47, v46
	v_fmac_f32_e32 v47, v48, v31
	v_fma_f32 v30, -v30, v47, v46
	v_div_fmas_f32 v30, v30, v31, v47
	v_div_fixup_f32 v28, v30, v28, 1.0
	v_add_u32_e32 v30, 0xa128, v64
	ds_read2_b32 v[30:31], v30 offset1:1
	v_pk_add_f32 v[8:9], v[8:9], v[28:29]
	s_waitcnt lgkmcnt(0)
	v_mul_f32_e32 v30, 0xbfb8aa3b, v30
	v_mul_f32_e32 v31, 0xbfb8aa3b, v31
	v_exp_f32_e32 v30, v30
	v_exp_f32_e32 v31, v31
	s_nop 0
	v_pk_add_f32 v[30:31], v[30:31], 1.0 op_sel_hi:[1,0]
	s_nop 0
	v_div_scale_f32 v46, s[0:1], v31, v31, 1.0
	v_rcp_f32_e32 v47, v46
	s_nop 0
	v_fma_f32 v48, -v46, v47, 1.0
	v_fmac_f32_e32 v47, v48, v47
	v_div_scale_f32 v48, vcc, 1.0, v31, 1.0
	v_mul_f32_e32 v49, v48, v47
	v_fma_f32 v51, -v46, v49, v48
	v_fmac_f32_e32 v49, v51, v47
	v_fma_f32 v46, -v46, v49, v48
	v_div_fmas_f32 v46, v46, v47, v49
	v_div_fixup_f32 v31, v46, v31, 1.0
	v_div_scale_f32 v46, s[0:1], v30, v30, 1.0
	v_rcp_f32_e32 v47, v46
	s_nop 0
	v_fma_f32 v48, -v46, v47, 1.0
	v_fmac_f32_e32 v47, v48, v47
	v_div_scale_f32 v48, vcc, 1.0, v30, 1.0
	v_mul_f32_e32 v49, v48, v47
	v_fma_f32 v51, -v46, v49, v48
	v_fmac_f32_e32 v49, v51, v47
	v_fma_f32 v46, -v46, v49, v48
	v_div_fmas_f32 v46, v46, v47, v49
	v_div_fixup_f32 v30, v46, v30, 1.0
	v_add_u32_e32 v46, 0xa130, v64
	ds_read2_b32 v[46:47], v46 offset1:1
	v_pk_add_f32 v[10:11], v[10:11], v[30:31]
	s_waitcnt lgkmcnt(0)
	v_mul_f32_e32 v46, 0xbfb8aa3b, v46
	v_mul_f32_e32 v47, 0xbfb8aa3b, v47
	v_exp_f32_e32 v46, v46
	v_exp_f32_e32 v47, v47
	s_nop 0
	v_pk_add_f32 v[46:47], v[46:47], 1.0 op_sel_hi:[1,0]
	s_nop 0
	v_div_scale_f32 v48, s[0:1], v47, v47, 1.0
	v_rcp_f32_e32 v49, v48
	s_nop 0
	v_fma_f32 v51, -v48, v49, 1.0
	v_fmac_f32_e32 v49, v51, v49
	v_div_scale_f32 v51, vcc, 1.0, v47, 1.0
	v_mul_f32_e32 v52, v51, v49
	v_fma_f32 v53, -v48, v52, v51
	v_fmac_f32_e32 v52, v53, v49
	v_fma_f32 v48, -v48, v52, v51
	v_div_fmas_f32 v48, v48, v49, v52
	v_div_fixup_f32 v47, v48, v47, 1.0
	v_div_scale_f32 v48, s[0:1], v46, v46, 1.0
	v_rcp_f32_e32 v49, v48
	s_nop 0
	v_fma_f32 v51, -v48, v49, 1.0
	v_fmac_f32_e32 v49, v51, v49
	v_div_scale_f32 v51, vcc, 1.0, v46, 1.0
	v_mul_f32_e32 v52, v51, v49
	v_fma_f32 v53, -v48, v52, v51
	v_fmac_f32_e32 v52, v53, v49
	v_fma_f32 v48, -v48, v52, v51
	v_div_fmas_f32 v48, v48, v49, v52
	v_div_fixup_f32 v46, v48, v46, 1.0
	v_add_u32_e32 v48, 0xa138, v64
	ds_read2_b32 v[48:49], v48 offset1:1
	v_pk_add_f32 v[4:5], v[4:5], v[46:47]
	s_waitcnt lgkmcnt(0)
	v_mul_f32_e32 v48, 0xbfb8aa3b, v48
	v_mul_f32_e32 v49, 0xbfb8aa3b, v49
	v_exp_f32_e32 v48, v48
	v_exp_f32_e32 v49, v49
	s_nop 0
	v_pk_add_f32 v[48:49], v[48:49], 1.0 op_sel_hi:[1,0]
	s_nop 0
	v_div_scale_f32 v51, s[0:1], v49, v49, 1.0
	v_rcp_f32_e32 v52, v51
	s_nop 0
	v_fma_f32 v53, -v51, v52, 1.0
	v_fmac_f32_e32 v52, v53, v52
	v_div_scale_f32 v53, vcc, 1.0, v49, 1.0
	v_mul_f32_e32 v54, v53, v52
	v_fma_f32 v55, -v51, v54, v53
	v_fmac_f32_e32 v54, v55, v52
	v_fma_f32 v51, -v51, v54, v53
	v_div_fmas_f32 v51, v51, v52, v54
	v_div_fixup_f32 v49, v51, v49, 1.0
	v_div_scale_f32 v51, s[0:1], v48, v48, 1.0
	v_rcp_f32_e32 v52, v51
	s_nop 0
	v_fma_f32 v53, -v51, v52, 1.0
	v_fmac_f32_e32 v52, v53, v52
	v_div_scale_f32 v53, vcc, 1.0, v48, 1.0
	v_mul_f32_e32 v54, v53, v52
	v_fma_f32 v55, -v51, v54, v53
	v_fmac_f32_e32 v54, v55, v52
	v_fma_f32 v51, -v51, v54, v53
	v_div_fmas_f32 v51, v51, v52, v54
	v_add_f32_e32 v54, v18, v23
	v_add_f32_e32 v55, v19, v22
	v_div_fixup_f32 v48, v51, v48, 1.0
	v_add_f32_e32 v51, v18, v19
	v_pk_add_f32 v[52:53], v[18:19], v[22:23]
	v_max_f32_e32 v54, v54, v55
	v_max3_f32 v51, v51, v52, v54
	v_add_f32_e32 v52, v22, v23
	v_max_f32_e32 v52, v53, v52
	v_max3_f32 v51, v51, v52, s4
	v_add_f32_e32 v54, v12, v13
	v_pk_add_f32 v[52:53], v[12:13], v[14:15]
	v_add_f32_e32 v55, v13, v14
	v_max_f32_e32 v52, v54, v52
	v_add_f32_e32 v54, v12, v15
	v_max_f32_e32 v54, v54, v55
	v_add_f32_e32 v55, v14, v15
	v_max_f32_e32 v53, v53, v55
	v_max3_f32 v52, v52, v54, v53
	v_cmp_gt_f32_e32 vcc, v52, v51
	v_add_f32_e32 v54, v8, v9
	v_add_f32_e32 v55, v9, v10
	v_cndmask_b32_e32 v51, v51, v52, vcc
	v_pk_add_f32 v[52:53], v[8:9], v[10:11]
	v_pk_add_f32 v[6:7], v[6:7], v[48:49]
	v_max_f32_e32 v52, v54, v52
	v_add_f32_e32 v54, v8, v11
	v_max_f32_e32 v54, v54, v55
	v_add_f32_e32 v55, v10, v11
	v_max_f32_e32 v53, v53, v55
	v_max3_f32 v52, v52, v54, v53
	v_cmp_gt_f32_e64 s[0:1], v52, v51
	v_add_f32_e32 v54, v4, v5
	v_add_f32_e32 v55, v5, v6
	v_cndmask_b32_e64 v51, v51, v52, s[0:1]
	v_pk_add_f32 v[52:53], v[4:5], v[6:7]
	s_nop 0
	v_max_f32_e32 v52, v54, v52
	v_add_f32_e32 v54, v4, v7
	v_max_f32_e32 v54, v54, v55
	v_add_f32_e32 v55, v6, v7
	v_max_f32_e32 v53, v53, v55
	v_max3_f32 v52, v52, v54, v53
	v_cmp_ngt_f32_e64 s[2:3], v52, v51
	v_cndmask_b32_e64 v51, 0, 1, vcc
	v_cndmask_b32_e64 v51, v51, 2, s[0:1]
	v_cndmask_b32_e64 v51, 3, v51, s[2:3]
	v_cmp_eq_u32_e32 vcc, 0, v51
	s_nop 1
	v_cndmask_b32_e32 v16, 0, v16, vcc
	v_cndmask_b32_e32 v17, 0, v17, vcc
	v_cndmask_b32_e32 v20, 0, v20, vcc
	v_cndmask_b32_e32 v21, 0, v21, vcc
	v_cndmask_b32_e32 v19, 0, v19, vcc
	v_cndmask_b32_e32 v18, 0, v18, vcc
	v_cndmask_b32_e32 v22, 0, v22, vcc
	v_cndmask_b32_e32 v23, 0, v23, vcc
	v_cmp_eq_u32_e32 vcc, 1, v51
	s_nop 1
	v_cndmask_b32_e32 v21, v21, v27, vcc
	v_cndmask_b32_e32 v20, v20, v26, vcc
	v_cndmask_b32_e32 v17, v17, v25, vcc
	v_cndmask_b32_e32 v16, v16, v24, vcc
	v_cndmask_b32_e32 v15, v23, v15, vcc
	v_cndmask_b32_e32 v14, v22, v14, vcc
	v_cndmask_b32_e32 v12, v18, v12, vcc
	v_cndmask_b32_e32 v13, v19, v13, vcc
	s_and_b64 vcc, s[0:1], s[2:3]
	v_cndmask_b32_e32 v9, v13, v9, vcc
	v_cndmask_b32_e32 v8, v12, v8, vcc
	v_cndmask_b32_e64 v4, v4, v8, s[2:3]
	v_cndmask_b32_e64 v5, v5, v9, s[2:3]
	v_cndmask_b32_e32 v16, v16, v28, vcc
	v_cndmask_b32_e32 v17, v17, v29, vcc
	v_cndmask_b32_e32 v18, v20, v30, vcc
	v_cndmask_b32_e32 v19, v21, v31, vcc
	v_cndmask_b32_e32 v10, v14, v10, vcc
	v_cndmask_b32_e32 v11, v15, v11, vcc
	v_cmp_gt_f32_e32 vcc, v5, v4
	v_cndmask_b32_e64 v6, v6, v10, s[2:3]
	v_cndmask_b32_e64 v7, v7, v11, s[2:3]
	v_cndmask_b32_e32 v9, v4, v5, vcc
	v_cndmask_b32_e64 v8, 0, 1, vcc
	v_cmp_gt_f32_e32 vcc, v6, v9
	v_cndmask_b32_e64 v12, v49, v19, s[2:3]
	v_cndmask_b32_e64 v13, v48, v18, s[2:3]
	v_cndmask_b32_e32 v9, v9, v6, vcc
	v_cndmask_b32_e64 v8, v8, 2, vcc
	v_cmp_ngt_f32_e64 s[0:1], v7, v9
	v_cndmask_b32_e64 v14, v47, v17, s[2:3]
	v_cndmask_b32_e64 v15, v46, v16, s[2:3]
	v_cndmask_b32_e64 v8, 3, v8, s[0:1]
	v_cmp_eq_u32_e64 s[2:3], 0, v8
	v_cmp_nlt_f32_e64 s[4:5], s4, v4
	s_or_b64 s[2:3], s[4:5], s[2:3]
	v_cndmask_b32_e64 v4, v4, v224, s[2:3]
	v_cndmask_b32_e64 v9, 0, -1, s[2:3]
	v_cmp_ne_u32_e64 s[2:3], 1, v8
	v_cmp_gt_f32_e64 s[4:5], v5, v4
	s_and_b64 s[2:3], s[2:3], s[4:5]
	v_cndmask_b32_e64 v4, v4, v5, s[2:3]
	v_cndmask_b32_e64 v9, v9, 1, s[2:3]
	s_and_b64 s[2:3], vcc, s[0:1]
	v_cmp_ngt_f32_e32 vcc, v6, v4
	s_or_b64 vcc, s[2:3], vcc
	s_nop 0
	v_cndmask_b32_e32 v4, v6, v4, vcc
	v_cndmask_b32_e32 v5, 2, v9, vcc
	v_cmp_gt_f32_e32 vcc, v7, v4
	s_and_b64 s[0:1], s[0:1], vcc
	v_cndmask_b32_e64 v4, v5, 3, s[0:1]
	v_min_i32_e32 v5, v8, v4
	v_max_i32_e32 v4, v8, v4
	v_cmp_eq_u32_e32 vcc, 0, v5
	v_subrev_co_u32_e64 v7, s[0:1], 1, v4
	s_nop 0
	v_cndmask_b32_e32 v6, 0, v15, vcc
	v_cndmask_b32_e64 v8, 0, v15, s[0:1]
	v_cmp_eq_u32_e64 s[0:1], 1, v5
	v_cmp_eq_u32_e64 s[2:3], 1, v4
	s_nop 0
	v_cndmask_b32_e64 v6, v6, v14, s[0:1]
	v_cndmask_b32_e64 v8, v8, v14, s[2:3]
	v_cmp_eq_u32_e64 s[2:3], 2, v5
	s_nop 1
	v_cndmask_b32_e64 v6, v6, v13, s[2:3]
	v_cmp_eq_u32_e64 s[2:3], 2, v4
	s_nop 1
	v_cndmask_b32_e64 v8, v8, v13, s[2:3]
	v_cmp_eq_u32_e64 s[2:3], 3, v5
	s_nop 1
	v_cndmask_b32_e64 v5, v6, v12, s[2:3]
	v_cmp_eq_u32_e64 s[2:3], 3, v4
	v_add_u32_e32 v4, 1, v4
	v_cndmask_b32_e64 v4, 5, v4, s[0:1]
	v_cndmask_b32_e64 v8, v8, v12, s[2:3]
	v_add_f32_e32 v6, v5, v8
	v_cndmask_b32_e32 v4, v4, v7, vcc
	v_div_scale_f32 v7, s[0:1], v6, v6, 1.0
	v_rcp_f32_e32 v9, v7
	s_nop 0
	v_fma_f32 v10, -v7, v9, 1.0
	v_fmac_f32_e32 v9, v10, v9
	v_div_scale_f32 v10, vcc, 1.0, v6, 1.0
	v_mul_f32_e32 v11, v10, v9
	v_fma_f32 v12, -v7, v11, v10
	v_fmac_f32_e32 v11, v12, v9
	v_fma_f32 v7, -v7, v11, v10
	v_div_fmas_f32 v7, v7, v9, v11
	v_div_fixup_f32 v7, v7, v6, 1.0
	v_mad_u32_u24 v6, v51, 6, v4
	v_mul_f32_e32 v4, v5, v7
	v_mul_f32_e32 v5, v8, v7
